# v1 + removed needless per-unit vmcnt(0) drain in non-gather GEMM loops + scalar-compare top-k search loop (2 tokens interleaved)
# speedup vs baseline: 1.0152x; 1.0086x over previous
;     __device__ __forceinline__ int arow(const pg8::Unit& u, int r) const { if (GATHER && u.roff >= 0) { const int rr = r < u.nvalid ? r : u.nvalid - 1; return tokl[u.roff + rr]; } return -u.roff - 1 + r; }
; template <class Epi, class Sched>
; __device__ __forceinline__ void gemm_phase(const int tid, LAS unsigned char* lds, const char* Abase, const int lda, const int ldb, const int K, const Sched& S, const Epi& E) {
;     ...
;             asm volatile("s_waitcnt vmcnt(0)" : "+v"(vAn[0][0]), "+v"(vAn[0][1]), "+v"(vAn[1][0]), "+v"(vAn[1][1]) :: "memory");
;             if constexpr (Epi::ROWSCALE) { asm volatile("" : "+v"(rs[0][0]), "+v"(rs[0][1]), "+v"(rs[0][2]), "+v"(rs[0][3]), "+v"(rs[1][0]), "+v"(rs[1][1]), "+v"(rs[1][2]), "+v"(rs[1][3])); }
;         } else { if (has_next) nA = Abase + (size_t)S.arow(nxt, 0) * lda + S.acolb(nxt); }
;         const char* nB = has_next ? nxt.bptr : cB;
;         int swb[2] = {0x7f7f7f7f, 0x7f7f7f7f}; if constexpr (Epi::F8MMA) { swb[0] = E.wscale(cur, 0); swb[1] = E.wscale(cur, 1); }
;     ...
; #pragma unroll
;         for (int a = 0; a < 2; ++a)
; #pragma unroll
;             for (int b = 0; b < 2; ++b)
; #pragma unroll
;                 for (int m = 0; m < 4; ++m)
; #pragma unroll
;                     for (int n = 0; n < 2; ++n) acc[a][b][m][n] = (f32x4){0.f, 0.f, 0.f, 0.f};
.LBB0_206:
	s_andn2_b64 vcc, exec, s[44:45]
	s_cbranch_vccnz .LBB0_217
	s_ashr_i32 s2, s73, 2
	s_mul_i32 s2, s2, 0xaaaaaaab
	s_add_i32 s2, s2, 0x2aaaaaaa
	s_cmp_lt_u32 s2, 0x55555555
	s_mov_b32 s2, 0x7a7a7a7a
	v_mov_b32_e32 v68, 0
	s_cselect_b32 s77, s2, 0x7b7b7b7b
	v_mov_b32_e32 v209, v3
	v_mov_b32_e32 v211, v3
	s_mov_b32 s78, 0
	s_mov_b64 s[2:3], 0x100
	v_mov_b32_e32 v69, v68
	v_mov_b32_e32 v70, v68
	s_waitcnt lgkmcnt(0)
	v_mov_b32_e32 v71, v68
	v_mov_b32_e32 v72, v68
	v_mov_b32_e32 v73, v68
	v_mov_b32_e32 v74, v68
	v_mov_b32_e32 v75, v68
	v_mov_b32_e32 v84, v68
	v_mov_b32_e32 v85, v68
	v_mov_b32_e32 v86, v68
	v_mov_b32_e32 v87, v68
	v_mov_b32_e32 v88, v68
	v_mov_b32_e32 v89, v68
	v_mov_b32_e32 v90, v68
	v_mov_b32_e32 v91, v68
	v_mov_b32_e32 v100, v68
	v_mov_b32_e32 v101, v68
	v_mov_b32_e32 v102, v68
	v_mov_b32_e32 v103, v68
	v_mov_b32_e32 v104, v68
	v_mov_b32_e32 v105, v68
	v_mov_b32_e32 v106, v68
	v_mov_b32_e32 v107, v68
	v_mov_b32_e32 v116, v68
	v_mov_b32_e32 v117, v68
	v_mov_b32_e32 v118, v68
	v_mov_b32_e32 v119, v68
	v_mov_b32_e32 v120, v68
	v_mov_b32_e32 v121, v68
	v_mov_b32_e32 v122, v68
	v_mov_b32_e32 v123, v68
	v_mov_b32_e32 v76, v68
	v_mov_b32_e32 v77, v68
	v_mov_b32_e32 v78, v68
	v_mov_b32_e32 v79, v68
	v_mov_b32_e32 v80, v68
	v_mov_b32_e32 v81, v68
	v_mov_b32_e32 v82, v68
	v_mov_b32_e32 v83, v68
	v_mov_b32_e32 v92, v68
	v_mov_b32_e32 v93, v68
	v_mov_b32_e32 v94, v68
	v_mov_b32_e32 v95, v68
	v_mov_b32_e32 v96, v68
	v_mov_b32_e32 v97, v68
	v_mov_b32_e32 v98, v68
	v_mov_b32_e32 v99, v68
	v_mov_b32_e32 v108, v68
	v_mov_b32_e32 v109, v68
	v_mov_b32_e32 v110, v68
	v_mov_b32_e32 v111, v68
	v_mov_b32_e32 v112, v68
	v_mov_b32_e32 v113, v68
	v_mov_b32_e32 v114, v68
	v_mov_b32_e32 v115, v68
	v_mov_b32_e32 v124, v68
	v_mov_b32_e32 v125, v68
	v_mov_b32_e32 v126, v68
	v_mov_b32_e32 v127, v68
	v_mov_b32_e32 v128, v68
	v_mov_b32_e32 v129, v68
	v_mov_b32_e32 v130, v68
	v_mov_b32_e32 v131, v68
	v_mov_b32_e32 v132, v68
	v_mov_b32_e32 v133, v68
	v_mov_b32_e32 v134, v68
	v_mov_b32_e32 v135, v68
	v_mov_b32_e32 v136, v68
	v_mov_b32_e32 v137, v68
	v_mov_b32_e32 v138, v68
	v_mov_b32_e32 v139, v68
	v_mov_b32_e32 v148, v68
	v_mov_b32_e32 v149, v68
	v_mov_b32_e32 v150, v68
	v_mov_b32_e32 v151, v68
	v_mov_b32_e32 v152, v68
	v_mov_b32_e32 v153, v68
	v_mov_b32_e32 v154, v68
	v_mov_b32_e32 v155, v68
	v_mov_b32_e32 v164, v68
	v_mov_b32_e32 v165, v68
	v_mov_b32_e32 v166, v68
	v_mov_b32_e32 v167, v68
	v_mov_b32_e32 v168, v68
	v_mov_b32_e32 v169, v68
	v_mov_b32_e32 v170, v68
	v_mov_b32_e32 v171, v68
	v_mov_b32_e32 v180, v68
	v_mov_b32_e32 v181, v68
	v_mov_b32_e32 v182, v68
	v_mov_b32_e32 v183, v68
	v_mov_b32_e32 v184, v68
	v_mov_b32_e32 v185, v68
	v_mov_b32_e32 v186, v68
	v_mov_b32_e32 v187, v68
	v_mov_b32_e32 v140, v68
	v_mov_b32_e32 v141, v68
	v_mov_b32_e32 v142, v68
	v_mov_b32_e32 v143, v68
	v_mov_b32_e32 v144, v68
	v_mov_b32_e32 v145, v68
	v_mov_b32_e32 v146, v68
	v_mov_b32_e32 v147, v68
	v_mov_b32_e32 v156, v68
	v_mov_b32_e32 v157, v68
	v_mov_b32_e32 v158, v68
	v_mov_b32_e32 v159, v68
	v_mov_b32_e32 v160, v68
	v_mov_b32_e32 v161, v68
	v_mov_b32_e32 v162, v68
	v_mov_b32_e32 v163, v68
	v_mov_b32_e32 v172, v68
	v_mov_b32_e32 v173, v68
	v_mov_b32_e32 v174, v68
	v_mov_b32_e32 v175, v68
	v_mov_b32_e32 v176, v68
	v_mov_b32_e32 v177, v68
	v_mov_b32_e32 v178, v68
	v_mov_b32_e32 v179, v68
	v_mov_b32_e32 v188, v68
	v_mov_b32_e32 v189, v68
	v_mov_b32_e32 v190, v68
	v_mov_b32_e32 v191, v68
	v_mov_b32_e32 v192, v68
	v_mov_b32_e32 v193, v68
	v_mov_b32_e32 v194, v68
	v_mov_b32_e32 v195, v68
	s_branch .LBB0_210

;     __device__ __forceinline__ int arow(const pg8::Unit& u, int r) const { if (GATHER && u.roff >= 0) { const int rr = r < u.nvalid ? r : u.nvalid - 1; return tokl[u.roff + rr]; } return -u.roff - 1 + r; }
; template <class Epi, class Sched>
; __device__ __forceinline__ void gemm_phase(const int tid, LAS unsigned char* lds, const char* Abase, const int lda, const int ldb, const int K, const Sched& S, const Epi& E) {
;     ...
;             asm volatile("s_waitcnt vmcnt(0)" : "+v"(vAn[0][0]), "+v"(vAn[0][1]), "+v"(vAn[1][0]), "+v"(vAn[1][1]) :: "memory");
;             if constexpr (Epi::ROWSCALE) { asm volatile("" : "+v"(rs[0][0]), "+v"(rs[0][1]), "+v"(rs[0][2]), "+v"(rs[0][3]), "+v"(rs[1][0]), "+v"(rs[1][1]), "+v"(rs[1][2]), "+v"(rs[1][3])); }
;         } else { if (has_next) nA = Abase + (size_t)S.arow(nxt, 0) * lda + S.acolb(nxt); }
;         const char* nB = has_next ? nxt.bptr : cB;
;         int swb[2] = {0x7f7f7f7f, 0x7f7f7f7f}; if constexpr (Epi::F8MMA) { swb[0] = E.wscale(cur, 0); swb[1] = E.wscale(cur, 1); }
;     ...
; #pragma unroll
;         for (int a = 0; a < 2; ++a)
; #pragma unroll
;             for (int b = 0; b < 2; ++b)
; #pragma unroll
;                 for (int m = 0; m < 4; ++m)
; #pragma unroll
;                     for (int n = 0; n < 2; ++n) acc[a][b][m][n] = (f32x4){0.f, 0.f, 0.f, 0.f};
.LBB0_661:
	s_andn2_b64 vcc, exec, s[46:47]
	s_cbranch_vccnz .LBB0_667
	v_mov_b32_e32 v68, 0
	v_mov_b32_e32 v209, v3
	v_mov_b32_e32 v211, v3
	s_mov_b32 s79, 0
	s_mov_b64 s[2:3], 0x100
	v_mov_b32_e32 v69, v68
	v_mov_b32_e32 v70, v68
	s_waitcnt lgkmcnt(0)
	v_mov_b32_e32 v71, v68
	v_mov_b32_e32 v72, v68
	v_mov_b32_e32 v73, v68
	v_mov_b32_e32 v74, v68
	v_mov_b32_e32 v75, v68
	v_mov_b32_e32 v84, v68
	v_mov_b32_e32 v85, v68
	v_mov_b32_e32 v86, v68
	v_mov_b32_e32 v87, v68
	v_mov_b32_e32 v88, v68
	v_mov_b32_e32 v89, v68
	v_mov_b32_e32 v90, v68
	v_mov_b32_e32 v91, v68
	v_mov_b32_e32 v100, v68
	v_mov_b32_e32 v101, v68
	v_mov_b32_e32 v102, v68
	v_mov_b32_e32 v103, v68
	v_mov_b32_e32 v104, v68
	v_mov_b32_e32 v105, v68
	v_mov_b32_e32 v106, v68
	v_mov_b32_e32 v107, v68
	v_mov_b32_e32 v116, v68
	v_mov_b32_e32 v117, v68
	v_mov_b32_e32 v118, v68
	v_mov_b32_e32 v119, v68
	v_mov_b32_e32 v120, v68
	v_mov_b32_e32 v121, v68
	v_mov_b32_e32 v122, v68
	v_mov_b32_e32 v123, v68
	v_mov_b32_e32 v76, v68
	v_mov_b32_e32 v77, v68
	v_mov_b32_e32 v78, v68
	v_mov_b32_e32 v79, v68
	v_mov_b32_e32 v80, v68
	v_mov_b32_e32 v81, v68
	v_mov_b32_e32 v82, v68
	v_mov_b32_e32 v83, v68
	v_mov_b32_e32 v92, v68
	v_mov_b32_e32 v93, v68
	v_mov_b32_e32 v94, v68
	v_mov_b32_e32 v95, v68
	v_mov_b32_e32 v96, v68
	v_mov_b32_e32 v97, v68
	v_mov_b32_e32 v98, v68
	v_mov_b32_e32 v99, v68
	v_mov_b32_e32 v108, v68
	v_mov_b32_e32 v109, v68
	v_mov_b32_e32 v110, v68
	v_mov_b32_e32 v111, v68
	v_mov_b32_e32 v112, v68
	v_mov_b32_e32 v113, v68
	v_mov_b32_e32 v114, v68
	v_mov_b32_e32 v115, v68
	v_mov_b32_e32 v124, v68
	v_mov_b32_e32 v125, v68
	v_mov_b32_e32 v126, v68
	v_mov_b32_e32 v127, v68
	v_mov_b32_e32 v128, v68
	v_mov_b32_e32 v129, v68
	v_mov_b32_e32 v130, v68
	v_mov_b32_e32 v131, v68
	v_mov_b32_e32 v132, v68
	v_mov_b32_e32 v133, v68
	v_mov_b32_e32 v134, v68
	v_mov_b32_e32 v135, v68
	v_mov_b32_e32 v136, v68
	v_mov_b32_e32 v137, v68
	v_mov_b32_e32 v138, v68
	v_mov_b32_e32 v139, v68
	v_mov_b32_e32 v148, v68
	v_mov_b32_e32 v149, v68
	v_mov_b32_e32 v150, v68
	v_mov_b32_e32 v151, v68
	v_mov_b32_e32 v152, v68
	v_mov_b32_e32 v153, v68
	v_mov_b32_e32 v154, v68
	v_mov_b32_e32 v155, v68
	v_mov_b32_e32 v164, v68
	v_mov_b32_e32 v165, v68
	v_mov_b32_e32 v166, v68
	v_mov_b32_e32 v167, v68
	v_mov_b32_e32 v168, v68
	v_mov_b32_e32 v169, v68
	v_mov_b32_e32 v170, v68
	v_mov_b32_e32 v171, v68
	v_mov_b32_e32 v180, v68
	v_mov_b32_e32 v181, v68
	v_mov_b32_e32 v182, v68
	v_mov_b32_e32 v183, v68
	v_mov_b32_e32 v184, v68
	v_mov_b32_e32 v185, v68
	v_mov_b32_e32 v186, v68
	v_mov_b32_e32 v187, v68
	v_mov_b32_e32 v140, v68
	v_mov_b32_e32 v141, v68
	v_mov_b32_e32 v142, v68
	v_mov_b32_e32 v143, v68
	v_mov_b32_e32 v144, v68
	v_mov_b32_e32 v145, v68
	v_mov_b32_e32 v146, v68
	v_mov_b32_e32 v147, v68
	v_mov_b32_e32 v156, v68
	v_mov_b32_e32 v157, v68
	v_mov_b32_e32 v158, v68
	v_mov_b32_e32 v159, v68
	v_mov_b32_e32 v160, v68
	v_mov_b32_e32 v161, v68
	v_mov_b32_e32 v162, v68
	v_mov_b32_e32 v163, v68
	v_mov_b32_e32 v172, v68
	v_mov_b32_e32 v173, v68
	v_mov_b32_e32 v174, v68
	v_mov_b32_e32 v175, v68
	v_mov_b32_e32 v176, v68
	v_mov_b32_e32 v177, v68
	v_mov_b32_e32 v178, v68
	v_mov_b32_e32 v179, v68
	v_mov_b32_e32 v188, v68
	v_mov_b32_e32 v189, v68
	v_mov_b32_e32 v190, v68
	v_mov_b32_e32 v191, v68
	v_mov_b32_e32 v192, v68
	v_mov_b32_e32 v193, v68
	v_mov_b32_e32 v194, v68
	v_mov_b32_e32 v195, v68
	s_branch .LBB0_665

;     __device__ __forceinline__ int arow(const pg8::Unit& u, int r) const { if (GATHER && u.roff >= 0) { const int rr = r < u.nvalid ? r : u.nvalid - 1; return tokl[u.roff + rr]; } return -u.roff - 1 + r; }
; template <class Epi, class Sched>
; __device__ __forceinline__ void gemm_phase(const int tid, LAS unsigned char* lds, const char* Abase, const int lda, const int ldb, const int K, const Sched& S, const Epi& E) {
;     ...
;             asm volatile("s_waitcnt vmcnt(0)" : "+v"(vAn[0][0]), "+v"(vAn[0][1]), "+v"(vAn[1][0]), "+v"(vAn[1][1]) :: "memory");
;             if constexpr (Epi::ROWSCALE) { asm volatile("" : "+v"(rs[0][0]), "+v"(rs[0][1]), "+v"(rs[0][2]), "+v"(rs[0][3]), "+v"(rs[1][0]), "+v"(rs[1][1]), "+v"(rs[1][2]), "+v"(rs[1][3])); }
;         } else { if (has_next) nA = Abase + (size_t)S.arow(nxt, 0) * lda + S.acolb(nxt); }
;         const char* nB = has_next ? nxt.bptr : cB;
;         int swb[2] = {0x7f7f7f7f, 0x7f7f7f7f}; if constexpr (Epi::F8MMA) { swb[0] = E.wscale(cur, 0); swb[1] = E.wscale(cur, 1); }
;     ...
; #pragma unroll
;         for (int a = 0; a < 2; ++a)
; #pragma unroll
;             for (int b = 0; b < 2; ++b)
; #pragma unroll
;                 for (int m = 0; m < 4; ++m)
; #pragma unroll
;                     for (int n = 0; n < 2; ++n) acc[a][b][m][n] = (f32x4){0.f, 0.f, 0.f, 0.f};
.LBB0_768:
	s_andn2_b64 vcc, exec, s[48:49]
	s_cbranch_vccnz .LBB0_774
	v_mov_b32_e32 v68, 0
	v_mov_b32_e32 v209, v3
	v_mov_b32_e32 v211, v3
	s_mov_b32 s83, 0
	s_mov_b64 s[2:3], 0x100
	v_mov_b32_e32 v69, v68
	v_mov_b32_e32 v70, v68
	s_waitcnt lgkmcnt(0)
	v_mov_b32_e32 v71, v68
	v_mov_b32_e32 v72, v68
	v_mov_b32_e32 v73, v68
	v_mov_b32_e32 v74, v68
	v_mov_b32_e32 v75, v68
	v_mov_b32_e32 v84, v68
	v_mov_b32_e32 v85, v68
	v_mov_b32_e32 v86, v68
	v_mov_b32_e32 v87, v68
	v_mov_b32_e32 v88, v68
	v_mov_b32_e32 v89, v68
	v_mov_b32_e32 v90, v68
	v_mov_b32_e32 v91, v68
	v_mov_b32_e32 v100, v68
	v_mov_b32_e32 v101, v68
	v_mov_b32_e32 v102, v68
	v_mov_b32_e32 v103, v68
	v_mov_b32_e32 v104, v68
	v_mov_b32_e32 v105, v68
	v_mov_b32_e32 v106, v68
	v_mov_b32_e32 v107, v68
	v_mov_b32_e32 v116, v68
	v_mov_b32_e32 v117, v68
	v_mov_b32_e32 v118, v68
	v_mov_b32_e32 v119, v68
	v_mov_b32_e32 v120, v68
	v_mov_b32_e32 v121, v68
	v_mov_b32_e32 v122, v68
	v_mov_b32_e32 v123, v68
	v_mov_b32_e32 v76, v68
	v_mov_b32_e32 v77, v68
	v_mov_b32_e32 v78, v68
	v_mov_b32_e32 v79, v68
	v_mov_b32_e32 v80, v68
	v_mov_b32_e32 v81, v68
	v_mov_b32_e32 v82, v68
	v_mov_b32_e32 v83, v68
	v_mov_b32_e32 v92, v68
	v_mov_b32_e32 v93, v68
	v_mov_b32_e32 v94, v68
	v_mov_b32_e32 v95, v68
	v_mov_b32_e32 v96, v68
	v_mov_b32_e32 v97, v68
	v_mov_b32_e32 v98, v68
	v_mov_b32_e32 v99, v68
	v_mov_b32_e32 v108, v68
	v_mov_b32_e32 v109, v68
	v_mov_b32_e32 v110, v68
	v_mov_b32_e32 v111, v68
	v_mov_b32_e32 v112, v68
	v_mov_b32_e32 v113, v68
	v_mov_b32_e32 v114, v68
	v_mov_b32_e32 v115, v68
	v_mov_b32_e32 v124, v68
	v_mov_b32_e32 v125, v68
	v_mov_b32_e32 v126, v68
	v_mov_b32_e32 v127, v68
	v_mov_b32_e32 v128, v68
	v_mov_b32_e32 v129, v68
	v_mov_b32_e32 v130, v68
	v_mov_b32_e32 v131, v68
	v_mov_b32_e32 v132, v68
	v_mov_b32_e32 v133, v68
	v_mov_b32_e32 v134, v68
	v_mov_b32_e32 v135, v68
	v_mov_b32_e32 v136, v68
	v_mov_b32_e32 v137, v68
	v_mov_b32_e32 v138, v68
	v_mov_b32_e32 v139, v68
	v_mov_b32_e32 v148, v68
	v_mov_b32_e32 v149, v68
	v_mov_b32_e32 v150, v68
	v_mov_b32_e32 v151, v68
	v_mov_b32_e32 v152, v68
	v_mov_b32_e32 v153, v68
	v_mov_b32_e32 v154, v68
	v_mov_b32_e32 v155, v68
	v_mov_b32_e32 v164, v68
	v_mov_b32_e32 v165, v68
	v_mov_b32_e32 v166, v68
	v_mov_b32_e32 v167, v68
	v_mov_b32_e32 v168, v68
	v_mov_b32_e32 v169, v68
	v_mov_b32_e32 v170, v68
	v_mov_b32_e32 v171, v68
	v_mov_b32_e32 v180, v68
	v_mov_b32_e32 v181, v68
	v_mov_b32_e32 v182, v68
	v_mov_b32_e32 v183, v68
	v_mov_b32_e32 v184, v68
	v_mov_b32_e32 v185, v68
	v_mov_b32_e32 v186, v68
	v_mov_b32_e32 v187, v68
	v_mov_b32_e32 v140, v68
	v_mov_b32_e32 v141, v68
	v_mov_b32_e32 v142, v68
	v_mov_b32_e32 v143, v68
	v_mov_b32_e32 v144, v68
	v_mov_b32_e32 v145, v68
	v_mov_b32_e32 v146, v68
	v_mov_b32_e32 v147, v68
	v_mov_b32_e32 v156, v68
	v_mov_b32_e32 v157, v68
	v_mov_b32_e32 v158, v68
	v_mov_b32_e32 v159, v68
	v_mov_b32_e32 v160, v68
	v_mov_b32_e32 v161, v68
	v_mov_b32_e32 v162, v68
	v_mov_b32_e32 v163, v68
	v_mov_b32_e32 v172, v68
	v_mov_b32_e32 v173, v68
	v_mov_b32_e32 v174, v68
	v_mov_b32_e32 v175, v68
	v_mov_b32_e32 v176, v68
	v_mov_b32_e32 v177, v68
	v_mov_b32_e32 v178, v68
	v_mov_b32_e32 v179, v68
	v_mov_b32_e32 v188, v68
	v_mov_b32_e32 v189, v68
	v_mov_b32_e32 v190, v68
	v_mov_b32_e32 v191, v68
	v_mov_b32_e32 v192, v68
	v_mov_b32_e32 v193, v68
	v_mov_b32_e32 v194, v68
	v_mov_b32_e32 v195, v68
	s_branch .LBB0_772

;     __device__ __forceinline__ int arow(const pg8::Unit& u, int r) const { if (GATHER && u.roff >= 0) { const int rr = r < u.nvalid ? r : u.nvalid - 1; return tokl[u.roff + rr]; } return -u.roff - 1 + r; }
; template <class Epi, class Sched>
; __device__ __forceinline__ void gemm_phase(const int tid, LAS unsigned char* lds, const char* Abase, const int lda, const int ldb, const int K, const Sched& S, const Epi& E) {
;     ...
;             asm volatile("s_waitcnt vmcnt(0)" : "+v"(vAn[0][0]), "+v"(vAn[0][1]), "+v"(vAn[1][0]), "+v"(vAn[1][1]) :: "memory");
;             if constexpr (Epi::ROWSCALE) { asm volatile("" : "+v"(rs[0][0]), "+v"(rs[0][1]), "+v"(rs[0][2]), "+v"(rs[0][3]), "+v"(rs[1][0]), "+v"(rs[1][1]), "+v"(rs[1][2]), "+v"(rs[1][3])); }
;         } else { if (has_next) nA = Abase + (size_t)S.arow(nxt, 0) * lda + S.acolb(nxt); }
;         const char* nB = has_next ? nxt.bptr : cB;
;         int swb[2] = {0x7f7f7f7f, 0x7f7f7f7f}; if constexpr (Epi::F8MMA) { swb[0] = E.wscale(cur, 0); swb[1] = E.wscale(cur, 1); }
;     ...
; #pragma unroll
;         for (int a = 0; a < 2; ++a)
; #pragma unroll
;             for (int b = 0; b < 2; ++b)
; #pragma unroll
;                 for (int m = 0; m < 4; ++m)
; #pragma unroll
;                     for (int n = 0; n < 2; ++n) acc[a][b][m][n] = (f32x4){0.f, 0.f, 0.f, 0.f};
.LBB0_1163:
	s_andn2_b64 vcc, exec, s[46:47]
	s_cbranch_vccnz .LBB0_1169
	v_mov_b32_e32 v68, 0
	v_mov_b32_e32 v207, v3
	v_mov_b32_e32 v209, v3
	s_mov_b32 s83, 0
	s_mov_b64 s[56:57], 0x100
	v_mov_b32_e32 v69, v68
	v_mov_b32_e32 v70, v68
	s_waitcnt lgkmcnt(0)
	v_mov_b32_e32 v71, v68
	v_mov_b32_e32 v72, v68
	v_mov_b32_e32 v73, v68
	v_mov_b32_e32 v74, v68
	v_mov_b32_e32 v75, v68
	v_mov_b32_e32 v84, v68
	v_mov_b32_e32 v85, v68
	v_mov_b32_e32 v86, v68
	v_mov_b32_e32 v87, v68
	v_mov_b32_e32 v88, v68
	v_mov_b32_e32 v89, v68
	v_mov_b32_e32 v90, v68
	v_mov_b32_e32 v91, v68
	v_mov_b32_e32 v100, v68
	v_mov_b32_e32 v101, v68
	v_mov_b32_e32 v102, v68
	v_mov_b32_e32 v103, v68
	v_mov_b32_e32 v104, v68
	v_mov_b32_e32 v105, v68
	v_mov_b32_e32 v106, v68
	v_mov_b32_e32 v107, v68
	v_mov_b32_e32 v116, v68
	v_mov_b32_e32 v117, v68
	v_mov_b32_e32 v118, v68
	v_mov_b32_e32 v119, v68
	v_mov_b32_e32 v120, v68
	v_mov_b32_e32 v121, v68
	v_mov_b32_e32 v122, v68
	v_mov_b32_e32 v123, v68
	v_mov_b32_e32 v76, v68
	v_mov_b32_e32 v77, v68
	v_mov_b32_e32 v78, v68
	v_mov_b32_e32 v79, v68
	v_mov_b32_e32 v80, v68
	v_mov_b32_e32 v81, v68
	v_mov_b32_e32 v82, v68
	v_mov_b32_e32 v83, v68
	v_mov_b32_e32 v92, v68
	v_mov_b32_e32 v93, v68
	v_mov_b32_e32 v94, v68
	v_mov_b32_e32 v95, v68
	v_mov_b32_e32 v96, v68
	v_mov_b32_e32 v97, v68
	v_mov_b32_e32 v98, v68
	v_mov_b32_e32 v99, v68
	v_mov_b32_e32 v108, v68
	v_mov_b32_e32 v109, v68
	v_mov_b32_e32 v110, v68
	v_mov_b32_e32 v111, v68
	v_mov_b32_e32 v112, v68
	v_mov_b32_e32 v113, v68
	v_mov_b32_e32 v114, v68
	v_mov_b32_e32 v115, v68
	v_mov_b32_e32 v124, v68
	v_mov_b32_e32 v125, v68
	v_mov_b32_e32 v126, v68
	v_mov_b32_e32 v127, v68
	v_mov_b32_e32 v128, v68
	v_mov_b32_e32 v129, v68
	v_mov_b32_e32 v130, v68
	v_mov_b32_e32 v131, v68
	v_mov_b32_e32 v132, v68
	v_mov_b32_e32 v133, v68
	v_mov_b32_e32 v134, v68
	v_mov_b32_e32 v135, v68
	v_mov_b32_e32 v136, v68
	v_mov_b32_e32 v137, v68
	v_mov_b32_e32 v138, v68
	v_mov_b32_e32 v139, v68
	v_mov_b32_e32 v148, v68
	v_mov_b32_e32 v149, v68
	v_mov_b32_e32 v150, v68
	v_mov_b32_e32 v151, v68
	v_mov_b32_e32 v152, v68
	v_mov_b32_e32 v153, v68
	v_mov_b32_e32 v154, v68
	v_mov_b32_e32 v155, v68
	v_mov_b32_e32 v164, v68
	v_mov_b32_e32 v165, v68
	v_mov_b32_e32 v166, v68
	v_mov_b32_e32 v167, v68
	v_mov_b32_e32 v168, v68
	v_mov_b32_e32 v169, v68
	v_mov_b32_e32 v170, v68
	v_mov_b32_e32 v171, v68
	v_mov_b32_e32 v180, v68
	v_mov_b32_e32 v181, v68
	v_mov_b32_e32 v182, v68
	v_mov_b32_e32 v183, v68
	v_mov_b32_e32 v184, v68
	v_mov_b32_e32 v185, v68
	v_mov_b32_e32 v186, v68
	v_mov_b32_e32 v187, v68
	v_mov_b32_e32 v140, v68
	v_mov_b32_e32 v141, v68
	v_mov_b32_e32 v142, v68
	v_mov_b32_e32 v143, v68
	v_mov_b32_e32 v144, v68
	v_mov_b32_e32 v145, v68
	v_mov_b32_e32 v146, v68
	v_mov_b32_e32 v147, v68
	v_mov_b32_e32 v156, v68
	v_mov_b32_e32 v157, v68
	v_mov_b32_e32 v158, v68
	v_mov_b32_e32 v159, v68
	v_mov_b32_e32 v160, v68
	v_mov_b32_e32 v161, v68
	v_mov_b32_e32 v162, v68
	v_mov_b32_e32 v163, v68
	v_mov_b32_e32 v172, v68
	v_mov_b32_e32 v173, v68
	v_mov_b32_e32 v174, v68
	v_mov_b32_e32 v175, v68
	v_mov_b32_e32 v176, v68
	v_mov_b32_e32 v177, v68
	v_mov_b32_e32 v178, v68
	v_mov_b32_e32 v179, v68
	v_mov_b32_e32 v188, v68
	v_mov_b32_e32 v189, v68
	v_mov_b32_e32 v190, v68
	v_mov_b32_e32 v191, v68
	v_mov_b32_e32 v192, v68
	v_mov_b32_e32 v193, v68
	v_mov_b32_e32 v194, v68
	v_mov_b32_e32 v195, v68
	s_branch .LBB0_1167

; #define LSTAMP(ty) do { if (blockIdx.x == 0 && F.tid == 0) { const unsigned long long now_ = __builtin_amdgcn_s_memrealtime(); LAS unsigned long long* st_ = (LAS unsigned long long*)(F.lc + 3072); \
;         st_[1 + (ty)] += now_ - st_[20]; st_[20] = now_; } } while (0)
; #define LSTAMP(ty) do { } while (0)
; #define LDS_ONLY_BARRIER() do { asm volatile("s_waitcnt lgkmcnt(0)" ::: "memory"); __builtin_amdgcn_s_barrier(); asm volatile("" ::: "memory"); } while (0)
; template <bool X16>
; __device__ __forceinline__ void ln1_router_phase(Frame& F, int layer, const float* xin) {
;     ...
;         unsigned tau[4] = {0u, 0u, 0u, 0u};
; #pragma unroll 1
;     ...
; #pragma unroll
;             for (int q = 0; q < 4; ++q) { const unsigned cand = tau[q] | (1u << bit); const int cnt = (int)__popcll(__ballot(key[q] >= cand)); tau[q] = (cnt >= TOPK) ? cand : tau[q]; } }
; #pragma unroll
;         for (int q = 0; q < 4; ++q) {
;             const unsigned long long gtm = __ballot(key[q] > tau[q]), eqm = __ballot(key[q] == tau[q]);
;             const int need = TOPK - (int)__popcll(gtm);
;             const unsigned long long below = (1ull << lane) - 1ull;
;             const bool ch = (key[q] > tau[q]) || ((key[q] == tau[q]) && ((int)__popcll(eqm & below) < need));
;             const unsigned long long chm = __ballot(ch);
;             const int rank = (int)__popcll(chm & below);
;             const float wsum = wave_sum(ch ? sgv[q] : 0.f);
;             wv[q] = sgv[q] / wsum * ROUTED_SCALE; rk[q] = rank; posl[q] = 0;
;             if (ch) { chosen_m |= (1 << q); posl[q] = __hip_atomic_fetch_add(lcnt + lane, 1, __ATOMIC_RELAXED, __HIP_MEMORY_SCOPE_WORKGROUP); }
;         }
;         LDS_ONLY_BARRIER();
;         LSTAMP(15);
;         if (wave == 0) { const int n = lcnt[lane]; int base = 0; if (n > 0) base = (int)__hip_atomic_fetch_add(gcnt + lane, (unsigned)n, RLX_AGENT); gb[lane] = base; }
.LBB0_1409:
	s_lshl_b32 s1, 1, s0
	s_or_b32 s57, s1, s9
	s_or_b32 s22, s1, s56
	v_cmp_le_u32_e32 vcc, s57, v69
	v_cmp_le_u32_e64 s[2:3], s22, v71
	s_bcnt1_i32_b64 vcc_lo, vcc
	s_bcnt1_i32_b64 s2, s[2:3]
	s_cmp_gt_u32 vcc_lo, 7
	s_cselect_b32 s9, s57, s9
	s_cmp_gt_u32 s2, 7
	s_cselect_b32 s56, s22, s56
	s_or_b32 s57, s1, s11
	s_or_b32 s22, s1, s10
	v_cmp_le_u32_e32 vcc, s57, v73
	v_cmp_le_u32_e64 s[2:3], s22, v74
	s_bcnt1_i32_b64 vcc_lo, vcc
	s_bcnt1_i32_b64 s2, s[2:3]
	s_cmp_gt_u32 vcc_lo, 7
	s_cselect_b32 s11, s57, s11
	s_cmp_gt_u32 s2, 7
	s_cselect_b32 s10, s22, s10
	s_add_i32 s0, s0, -1
	s_cmp_eq_u32 s0, -1
	s_cbranch_scc0 .LBB0_1409
	v_cmp_eq_u32_e64 s[0:1], s9, v69
	v_cmp_lt_u32_e32 vcc, s9, v69
	s_bcnt1_i32_b64 s2, vcc
	v_and_b32_e32 v72, s0, v92
	v_and_b32_e32 v69, s1, v1
	v_bcnt_u32_b32 v72, v72, 0
	s_sub_i32 s2, 8, s2
	v_bcnt_u32_b32 v69, v69, v72
	v_cmp_gt_i32_e64 s[2:3], s2, v69
	s_and_b64 s[0:1], s[0:1], s[2:3]
	s_or_b64 vcc, vcc, s[0:1]
	v_cndmask_b32_e32 v72, 0, v85, vcc
	ds_bpermute_b32 v75, v159, v72
	v_cndmask_b32_e64 v69, 0, 1, vcc
	v_cmp_ne_u32_e64 s[62:63], 0, v69
	v_mov_b32_e32 v77, 0
	v_mov_b32_e32 v69, 0
	s_waitcnt lgkmcnt(0)
	v_add_f32_e32 v72, v72, v75
	ds_bpermute_b32 v75, v160, v72
	s_waitcnt lgkmcnt(0)
	v_add_f32_e32 v72, v72, v75
	ds_bpermute_b32 v75, v161, v72
	s_waitcnt lgkmcnt(0)
	v_add_f32_e32 v72, v72, v75
	ds_bpermute_b32 v75, v162, v72
	s_waitcnt lgkmcnt(0)
	v_add_f32_e32 v72, v72, v75
	ds_bpermute_b32 v75, v163, v72
	s_waitcnt lgkmcnt(0)
	v_add_f32_e32 v82, v72, v75
	ds_bpermute_b32 v83, v164, v82
	v_mov_b32_e32 v72, 0
	s_and_saveexec_b64 s[0:1], vcc
	v_mov_b32_e32 v69, 1
	ds_add_rtn_u32 v77, v156, v69
	s_or_b64 exec, exec, s[0:1]
	v_cmp_eq_u32_e64 s[0:1], s56, v71
	v_cmp_lt_u32_e32 vcc, s56, v71
	s_bcnt1_i32_b64 s2, vcc
	v_and_b32_e32 v75, s0, v92
	v_and_b32_e32 v71, s1, v1
	v_bcnt_u32_b32 v75, v75, 0
	s_sub_i32 s2, 8, s2
	v_bcnt_u32_b32 v71, v71, v75
	v_cmp_gt_i32_e64 s[2:3], s2, v71
	s_and_b64 s[0:1], s[0:1], s[2:3]
	s_or_b64 vcc, vcc, s[0:1]
	v_cndmask_b32_e64 v71, 0, 1, vcc
	v_cmp_ne_u32_e64 s[56:57], 0, v71
	v_cndmask_b32_e32 v71, 0, v2, vcc
	ds_bpermute_b32 v75, v159, v71
	s_waitcnt lgkmcnt(0)
	v_add_f32_e32 v71, v71, v75
	ds_bpermute_b32 v75, v160, v71
	s_waitcnt lgkmcnt(0)
	v_add_f32_e32 v71, v71, v75
	ds_bpermute_b32 v75, v161, v71
	s_waitcnt lgkmcnt(0)
	v_add_f32_e32 v71, v71, v75
	ds_bpermute_b32 v75, v162, v71
	s_waitcnt lgkmcnt(0)
	v_add_f32_e32 v71, v71, v75
	ds_bpermute_b32 v75, v163, v71
	s_waitcnt lgkmcnt(0)
	v_add_f32_e32 v80, v71, v75
	ds_bpermute_b32 v81, v164, v80
	s_and_saveexec_b64 s[0:1], vcc
	ds_add_rtn_u32 v72, v156, v217
	v_or_b32_e32 v69, 2, v69
	s_or_b64 exec, exec, s[0:1]
	v_cmp_eq_u32_e64 s[0:1], s11, v73
	v_cmp_lt_u32_e32 vcc, s11, v73
	s_bcnt1_i32_b64 s2, vcc
	v_and_b32_e32 v73, s0, v92
	v_and_b32_e32 v71, s1, v1
	v_bcnt_u32_b32 v73, v73, 0
	s_sub_i32 s2, 8, s2
	v_bcnt_u32_b32 v71, v71, v73
	v_cmp_gt_i32_e64 s[2:3], s2, v71
	s_and_b64 s[0:1], s[0:1], s[2:3]
	s_or_b64 vcc, vcc, s[0:1]
	v_cndmask_b32_e32 v71, 0, v68, vcc
	ds_bpermute_b32 v75, v159, v71
	v_cndmask_b32_e64 v73, 0, 1, vcc
	v_cmp_ne_u32_e64 s[60:61], 0, v73
	s_waitcnt lgkmcnt(0)
	v_add_f32_e32 v71, v71, v75
	ds_bpermute_b32 v75, v160, v71
	s_waitcnt lgkmcnt(0)
	v_add_f32_e32 v71, v71, v75
	ds_bpermute_b32 v75, v161, v71
	s_waitcnt lgkmcnt(0)
	v_add_f32_e32 v71, v71, v75
	ds_bpermute_b32 v75, v162, v71
	s_waitcnt lgkmcnt(0)
	v_add_f32_e32 v71, v71, v75
	ds_bpermute_b32 v75, v163, v71
	s_waitcnt lgkmcnt(0)
	v_add_f32_e32 v76, v71, v75
	ds_bpermute_b32 v78, v164, v76
	v_mov_b32_e32 v71, 0
	v_mov_b32_e32 v75, 0
	s_and_saveexec_b64 s[0:1], vcc
	ds_add_rtn_u32 v75, v156, v217
	v_or_b32_e32 v69, 4, v69
	s_or_b64 exec, exec, s[0:1]
	v_cmp_eq_u32_e64 s[0:1], s10, v74
	v_cmp_lt_u32_e32 vcc, s10, v74
	s_bcnt1_i32_b64 s2, vcc
	v_and_b32_e32 v74, s0, v92
	v_and_b32_e32 v73, s1, v1
	v_bcnt_u32_b32 v74, v74, 0
	s_sub_i32 s2, 8, s2
	v_bcnt_u32_b32 v73, v73, v74
	v_cmp_gt_i32_e64 s[2:3], s2, v73
	s_and_b64 s[0:1], s[0:1], s[2:3]
	s_or_b64 vcc, vcc, s[0:1]
	v_cndmask_b32_e64 v73, 0, 1, vcc
	v_cmp_ne_u32_e64 s[0:1], 0, v73
	v_cndmask_b32_e32 v73, 0, v70, vcc
	ds_bpermute_b32 v74, v159, v73
	s_waitcnt lgkmcnt(0)
	v_add_f32_e32 v73, v73, v74
	ds_bpermute_b32 v74, v160, v73
	s_waitcnt lgkmcnt(0)
	v_add_f32_e32 v73, v73, v74
	ds_bpermute_b32 v74, v161, v73
	s_waitcnt lgkmcnt(0)
	v_add_f32_e32 v73, v73, v74
	ds_bpermute_b32 v74, v162, v73
	s_waitcnt lgkmcnt(0)
	v_add_f32_e32 v73, v73, v74
	ds_bpermute_b32 v74, v163, v73
	s_waitcnt lgkmcnt(0)
	v_add_f32_e32 v73, v73, v74
	ds_bpermute_b32 v74, v164, v73
	s_and_saveexec_b64 s[2:3], vcc
	ds_add_rtn_u32 v71, v156, v217
	v_or_b32_e32 v69, 8, v69
	s_or_b64 exec, exec, s[2:3]
	s_waitcnt lgkmcnt(0)
	s_barrier
	s_andn2_b64 vcc, exec, s[68:69]
	s_cbranch_vccnz .LBB0_1422
	ds_read_b32 v108, v156
	v_mov_b32_e32 v79, 0
	s_waitcnt lgkmcnt(0)
	v_cmp_lt_i32_e32 vcc, 0, v108
	s_and_saveexec_b64 s[2:3], vcc
	s_cbranch_execz .LBB0_1421
	global_atomic_add v79, v[94:95], v108, off sc0

; #define LSTAMP(ty) do { if (blockIdx.x == 0 && F.tid == 0) { const unsigned long long now_ = __builtin_amdgcn_s_memrealtime(); LAS unsigned long long* st_ = (LAS unsigned long long*)(F.lc + 3072); \
;         st_[1 + (ty)] += now_ - st_[20]; st_[20] = now_; } } while (0)
; #define LSTAMP(ty) do { } while (0)
; #define LDS_ONLY_BARRIER() do { asm volatile("s_waitcnt lgkmcnt(0)" ::: "memory"); __builtin_amdgcn_s_barrier(); asm volatile("" ::: "memory"); } while (0)
; template <bool X16>
; __device__ __forceinline__ void ln1_router_phase(Frame& F, int layer, const float* xin) {
;     ...
;         unsigned tau[4] = {0u, 0u, 0u, 0u};
; #pragma unroll 1
;     ...
; #pragma unroll
;             for (int q = 0; q < 4; ++q) { const unsigned cand = tau[q] | (1u << bit); const int cnt = (int)__popcll(__ballot(key[q] >= cand)); tau[q] = (cnt >= TOPK) ? cand : tau[q]; } }
; #pragma unroll
;         for (int q = 0; q < 4; ++q) {
;             const unsigned long long gtm = __ballot(key[q] > tau[q]), eqm = __ballot(key[q] == tau[q]);
;             const int need = TOPK - (int)__popcll(gtm);
;             const unsigned long long below = (1ull << lane) - 1ull;
;             const bool ch = (key[q] > tau[q]) || ((key[q] == tau[q]) && ((int)__popcll(eqm & below) < need));
;             const unsigned long long chm = __ballot(ch);
;             const int rank = (int)__popcll(chm & below);
;             const float wsum = wave_sum(ch ? sgv[q] : 0.f);
;             wv[q] = sgv[q] / wsum * ROUTED_SCALE; rk[q] = rank; posl[q] = 0;
;             if (ch) { chosen_m |= (1 << q); posl[q] = __hip_atomic_fetch_add(lcnt + lane, 1, __ATOMIC_RELAXED, __HIP_MEMORY_SCOPE_WORKGROUP); }
;         }
;         LDS_ONLY_BARRIER();
;         LSTAMP(15);
;         if (wave == 0) { const int n = lcnt[lane]; int base = 0; if (n > 0) base = (int)__hip_atomic_fetch_add(gcnt + lane, (unsigned)n, RLX_AGENT); gb[lane] = base; }
.LBB0_1453:
	s_lshl_b32 s1, 1, s0
	s_or_b32 s54, s1, s9
	s_or_b32 s22, s1, s29
	v_cmp_le_u32_e32 vcc, s54, v5
	v_cmp_le_u32_e64 s[2:3], s22, v123
	s_bcnt1_i32_b64 vcc_lo, vcc
	s_bcnt1_i32_b64 s2, s[2:3]
	s_cmp_gt_u32 vcc_lo, 7
	s_cselect_b32 s9, s54, s9
	s_cmp_gt_u32 s2, 7
	s_cselect_b32 s29, s22, s29
	s_or_b32 s54, s1, s11
	s_or_b32 s22, s1, s10
	v_cmp_le_u32_e32 vcc, s54, v125
	v_cmp_le_u32_e64 s[2:3], s22, v126
	s_bcnt1_i32_b64 vcc_lo, vcc
	s_bcnt1_i32_b64 s2, s[2:3]
	s_cmp_gt_u32 vcc_lo, 7
	s_cselect_b32 s11, s54, s11
	s_cmp_gt_u32 s2, 7
	s_cselect_b32 s10, s22, s10
	s_add_i32 s0, s0, -1
	s_cmp_eq_u32 s0, -1
	s_cbranch_scc0 .LBB0_1453
	v_cmp_eq_u32_e64 s[0:1], s9, v5
	v_cmp_lt_u32_e32 vcc, s9, v5
	s_bcnt1_i32_b64 s2, vcc
	v_and_b32_e32 v124, s0, v106
	v_and_b32_e32 v5, s1, v1
	v_bcnt_u32_b32 v124, v124, 0
	s_sub_i32 s2, 8, s2
	v_bcnt_u32_b32 v5, v5, v124
	v_cmp_gt_i32_e64 s[2:3], s2, v5
	s_and_b64 s[0:1], s[0:1], s[2:3]
	s_or_b64 vcc, vcc, s[0:1]
	v_cndmask_b32_e32 v124, 0, v177, vcc
	ds_bpermute_b32 v127, v144, v124
	v_cndmask_b32_e64 v5, 0, 1, vcc
	v_cmp_ne_u32_e64 s[60:61], 0, v5
	v_mov_b32_e32 v129, 0
	v_mov_b32_e32 v5, 0
	s_waitcnt lgkmcnt(0)
	v_add_f32_e32 v124, v124, v127
	ds_bpermute_b32 v127, v145, v124
	s_waitcnt lgkmcnt(0)
	v_add_f32_e32 v124, v124, v127
	ds_bpermute_b32 v127, v146, v124
	s_waitcnt lgkmcnt(0)
	v_add_f32_e32 v124, v124, v127
	ds_bpermute_b32 v127, v147, v124
	s_waitcnt lgkmcnt(0)
	v_add_f32_e32 v124, v124, v127
	ds_bpermute_b32 v127, v148, v124
	s_waitcnt lgkmcnt(0)
	v_add_f32_e32 v134, v124, v127
	ds_bpermute_b32 v135, v149, v134
	v_mov_b32_e32 v124, 0
	s_and_saveexec_b64 s[0:1], vcc
	v_mov_b32_e32 v5, 1
	ds_add_rtn_u32 v129, v141, v5
	s_or_b64 exec, exec, s[0:1]
	v_cmp_eq_u32_e64 s[0:1], s29, v123
	v_cmp_lt_u32_e32 vcc, s29, v123
	s_bcnt1_i32_b64 s2, vcc
	v_and_b32_e32 v127, s0, v106
	v_and_b32_e32 v123, s1, v1
	v_bcnt_u32_b32 v127, v127, 0
	s_sub_i32 s2, 8, s2
	v_bcnt_u32_b32 v123, v123, v127
	v_cmp_gt_i32_e64 s[2:3], s2, v123
	s_and_b64 s[0:1], s[0:1], s[2:3]
	s_or_b64 vcc, vcc, s[0:1]
	v_cndmask_b32_e64 v123, 0, 1, vcc
	v_cmp_ne_u32_e64 s[54:55], 0, v123
	v_cndmask_b32_e32 v123, 0, v2, vcc
	ds_bpermute_b32 v127, v144, v123
	s_waitcnt lgkmcnt(0)
	v_add_f32_e32 v123, v123, v127
	ds_bpermute_b32 v127, v145, v123
	s_waitcnt lgkmcnt(0)
	v_add_f32_e32 v123, v123, v127
	ds_bpermute_b32 v127, v146, v123
	s_waitcnt lgkmcnt(0)
	v_add_f32_e32 v123, v123, v127
	ds_bpermute_b32 v127, v147, v123
	s_waitcnt lgkmcnt(0)
	v_add_f32_e32 v123, v123, v127
	ds_bpermute_b32 v127, v148, v123
	s_waitcnt lgkmcnt(0)
	v_add_f32_e32 v132, v123, v127
	ds_bpermute_b32 v133, v149, v132
	s_and_saveexec_b64 s[0:1], vcc
	ds_add_rtn_u32 v124, v141, v217
	v_or_b32_e32 v5, 2, v5
	s_or_b64 exec, exec, s[0:1]
	v_cmp_eq_u32_e64 s[0:1], s11, v125
	v_cmp_lt_u32_e32 vcc, s11, v125
	s_bcnt1_i32_b64 s2, vcc
	v_and_b32_e32 v125, s0, v106
	v_and_b32_e32 v123, s1, v1
	v_bcnt_u32_b32 v125, v125, 0
	s_sub_i32 s2, 8, s2
	v_bcnt_u32_b32 v123, v123, v125
	v_cmp_gt_i32_e64 s[2:3], s2, v123
	s_and_b64 s[0:1], s[0:1], s[2:3]
	s_or_b64 vcc, vcc, s[0:1]
	v_cndmask_b32_e32 v123, 0, v4, vcc
	ds_bpermute_b32 v127, v144, v123
	v_cndmask_b32_e64 v125, 0, 1, vcc
	v_cmp_ne_u32_e64 s[56:57], 0, v125
	s_waitcnt lgkmcnt(0)
	v_add_f32_e32 v123, v123, v127
	ds_bpermute_b32 v127, v145, v123
	s_waitcnt lgkmcnt(0)
	v_add_f32_e32 v123, v123, v127
	ds_bpermute_b32 v127, v146, v123
	s_waitcnt lgkmcnt(0)
	v_add_f32_e32 v123, v123, v127
	ds_bpermute_b32 v127, v147, v123
	s_waitcnt lgkmcnt(0)
	v_add_f32_e32 v123, v123, v127
	ds_bpermute_b32 v127, v148, v123
	s_waitcnt lgkmcnt(0)
	v_add_f32_e32 v128, v123, v127
	ds_bpermute_b32 v130, v149, v128
	v_mov_b32_e32 v123, 0
	v_mov_b32_e32 v127, 0
	s_and_saveexec_b64 s[0:1], vcc
	ds_add_rtn_u32 v127, v141, v217
	v_or_b32_e32 v5, 4, v5
	s_or_b64 exec, exec, s[0:1]
	v_cmp_eq_u32_e64 s[0:1], s10, v126
	v_cmp_lt_u32_e32 vcc, s10, v126
	s_bcnt1_i32_b64 s2, vcc
	v_and_b32_e32 v126, s0, v106
	v_and_b32_e32 v125, s1, v1
	v_bcnt_u32_b32 v126, v126, 0
	s_sub_i32 s2, 8, s2
	v_bcnt_u32_b32 v125, v125, v126
	v_cmp_gt_i32_e64 s[2:3], s2, v125
	s_and_b64 s[0:1], s[0:1], s[2:3]
	s_or_b64 vcc, vcc, s[0:1]
	v_cndmask_b32_e64 v125, 0, 1, vcc
	v_cmp_ne_u32_e64 s[0:1], 0, v125
	v_cndmask_b32_e32 v125, 0, v122, vcc
	ds_bpermute_b32 v126, v144, v125
	s_waitcnt lgkmcnt(0)
	v_add_f32_e32 v125, v125, v126
	ds_bpermute_b32 v126, v145, v125
	s_waitcnt lgkmcnt(0)
	v_add_f32_e32 v125, v125, v126
	ds_bpermute_b32 v126, v146, v125
	s_waitcnt lgkmcnt(0)
	v_add_f32_e32 v125, v125, v126
	ds_bpermute_b32 v126, v147, v125
	s_waitcnt lgkmcnt(0)
	v_add_f32_e32 v125, v125, v126
	ds_bpermute_b32 v126, v148, v125
	s_waitcnt lgkmcnt(0)
	v_add_f32_e32 v125, v125, v126
	ds_bpermute_b32 v126, v149, v125
	s_and_saveexec_b64 s[2:3], vcc
	ds_add_rtn_u32 v123, v141, v217
	v_or_b32_e32 v5, 8, v5
	s_or_b64 exec, exec, s[2:3]
	s_waitcnt lgkmcnt(0)
	s_barrier
	s_andn2_b64 vcc, exec, s[62:63]
	s_cbranch_vccnz .LBB0_1466
	ds_read_b32 v136, v141
	v_mov_b32_e32 v131, 0
	s_waitcnt lgkmcnt(0)
	v_cmp_lt_i32_e32 vcc, 0, v136
	s_and_saveexec_b64 s[2:3], vcc
	s_cbranch_execz .LBB0_1465
	global_atomic_add v131, v[108:109], v136, off sc0

;     __device__ __forceinline__ int arow(const pg8::Unit& u, int r) const { if (GATHER && u.roff >= 0) { const int rr = r < u.nvalid ? r : u.nvalid - 1; return tokl[u.roff + rr]; } return -u.roff - 1 + r; }
; template <class Epi, class Sched>
; __device__ __forceinline__ void gemm_phase(const int tid, LAS unsigned char* lds, const char* Abase, const int lda, const int ldb, const int K, const Sched& S, const Epi& E) {
;     ...
;             asm volatile("s_waitcnt vmcnt(0)" : "+v"(vAn[0][0]), "+v"(vAn[0][1]), "+v"(vAn[1][0]), "+v"(vAn[1][1]) :: "memory");
;             if constexpr (Epi::ROWSCALE) { asm volatile("" : "+v"(rs[0][0]), "+v"(rs[0][1]), "+v"(rs[0][2]), "+v"(rs[0][3]), "+v"(rs[1][0]), "+v"(rs[1][1]), "+v"(rs[1][2]), "+v"(rs[1][3])); }
;         } else { if (has_next) nA = Abase + (size_t)S.arow(nxt, 0) * lda + S.acolb(nxt); }
;         const char* nB = has_next ? nxt.bptr : cB;
;         int swb[2] = {0x7f7f7f7f, 0x7f7f7f7f}; if constexpr (Epi::F8MMA) { swb[0] = E.wscale(cur, 0); swb[1] = E.wscale(cur, 1); }
;     ...
; #pragma unroll
;         for (int a = 0; a < 2; ++a)
; #pragma unroll
;             for (int b = 0; b < 2; ++b)
; #pragma unroll
;                 for (int m = 0; m < 4; ++m)
; #pragma unroll
;                     for (int n = 0; n < 2; ++n) acc[a][b][m][n] = (f32x4){0.f, 0.f, 0.f, 0.f};
.LBB0_1705:
	s_andn2_b64 vcc, exec, s[46:47]
	s_cbranch_vccnz .LBB0_1716
	s_add_u32 s87, s56, 0x100
	v_mov_b32_e32 v68, 0
	v_mov_b32_e32 v209, v3
	v_mov_b32_e32 v207, v3
	s_addc_u32 s88, s57, 0
	s_mov_b32 s89, 0
	s_mov_b64 s[56:57], 0x10000
	v_mov_b32_e32 v69, v68
	v_mov_b32_e32 v70, v68
	v_mov_b32_e32 v71, v68
	v_mov_b32_e32 v72, v68
	v_mov_b32_e32 v73, v68
	v_mov_b32_e32 v74, v68
	v_mov_b32_e32 v75, v68
	v_mov_b32_e32 v84, v68
	v_mov_b32_e32 v85, v68
	v_mov_b32_e32 v86, v68
	v_mov_b32_e32 v87, v68
	v_mov_b32_e32 v88, v68
	v_mov_b32_e32 v89, v68
	v_mov_b32_e32 v90, v68
	v_mov_b32_e32 v91, v68
	v_mov_b32_e32 v100, v68
	v_mov_b32_e32 v101, v68
	v_mov_b32_e32 v102, v68
	v_mov_b32_e32 v103, v68
	v_mov_b32_e32 v104, v68
	v_mov_b32_e32 v105, v68
	v_mov_b32_e32 v106, v68
	v_mov_b32_e32 v107, v68
	v_mov_b32_e32 v116, v68
	v_mov_b32_e32 v117, v68
	v_mov_b32_e32 v118, v68
	v_mov_b32_e32 v119, v68
	v_mov_b32_e32 v120, v68
	v_mov_b32_e32 v121, v68
	v_mov_b32_e32 v122, v68
	v_mov_b32_e32 v123, v68
	v_mov_b32_e32 v76, v68
	v_mov_b32_e32 v77, v68
	v_mov_b32_e32 v78, v68
	v_mov_b32_e32 v79, v68
	v_mov_b32_e32 v80, v68
	v_mov_b32_e32 v81, v68
	v_mov_b32_e32 v82, v68
	v_mov_b32_e32 v83, v68
	v_mov_b32_e32 v92, v68
	v_mov_b32_e32 v93, v68
	v_mov_b32_e32 v94, v68
	v_mov_b32_e32 v95, v68
	v_mov_b32_e32 v96, v68
	v_mov_b32_e32 v97, v68
	v_mov_b32_e32 v98, v68
	v_mov_b32_e32 v99, v68
	v_mov_b32_e32 v108, v68
	v_mov_b32_e32 v109, v68
	v_mov_b32_e32 v110, v68
	v_mov_b32_e32 v111, v68
	v_mov_b32_e32 v112, v68
	v_mov_b32_e32 v113, v68
	v_mov_b32_e32 v114, v68
	v_mov_b32_e32 v115, v68
	v_mov_b32_e32 v124, v68
	v_mov_b32_e32 v125, v68
	v_mov_b32_e32 v126, v68
	v_mov_b32_e32 v127, v68
	v_mov_b32_e32 v128, v68
	v_mov_b32_e32 v129, v68
	v_mov_b32_e32 v130, v68
	v_mov_b32_e32 v131, v68
	v_mov_b32_e32 v132, v68
	v_mov_b32_e32 v133, v68
	v_mov_b32_e32 v134, v68
	v_mov_b32_e32 v135, v68
	v_mov_b32_e32 v136, v68
	v_mov_b32_e32 v137, v68
	v_mov_b32_e32 v138, v68
	v_mov_b32_e32 v139, v68
	v_mov_b32_e32 v148, v68
	v_mov_b32_e32 v149, v68
	v_mov_b32_e32 v150, v68
	v_mov_b32_e32 v151, v68
	v_mov_b32_e32 v152, v68
	v_mov_b32_e32 v153, v68
	v_mov_b32_e32 v154, v68
	v_mov_b32_e32 v155, v68
	v_mov_b32_e32 v164, v68
	v_mov_b32_e32 v165, v68
	v_mov_b32_e32 v166, v68
	v_mov_b32_e32 v167, v68
	v_mov_b32_e32 v168, v68
	v_mov_b32_e32 v169, v68
	v_mov_b32_e32 v170, v68
	v_mov_b32_e32 v171, v68
	v_mov_b32_e32 v180, v68
	v_mov_b32_e32 v181, v68
	v_mov_b32_e32 v182, v68
	v_mov_b32_e32 v183, v68
	v_mov_b32_e32 v184, v68
	v_mov_b32_e32 v185, v68
	v_mov_b32_e32 v186, v68
	v_mov_b32_e32 v187, v68
	v_mov_b32_e32 v140, v68
	v_mov_b32_e32 v141, v68
	v_mov_b32_e32 v142, v68
	v_mov_b32_e32 v143, v68
	v_mov_b32_e32 v144, v68
	v_mov_b32_e32 v145, v68
	v_mov_b32_e32 v146, v68
	v_mov_b32_e32 v147, v68
	v_mov_b32_e32 v156, v68
	v_mov_b32_e32 v157, v68
	v_mov_b32_e32 v158, v68
	v_mov_b32_e32 v159, v68
	v_mov_b32_e32 v160, v68
	v_mov_b32_e32 v161, v68
	v_mov_b32_e32 v162, v68
	v_mov_b32_e32 v163, v68
	v_mov_b32_e32 v172, v68
	v_mov_b32_e32 v173, v68
	v_mov_b32_e32 v174, v68
	v_mov_b32_e32 v175, v68
	v_mov_b32_e32 v176, v68
	v_mov_b32_e32 v177, v68
	v_mov_b32_e32 v178, v68
	v_mov_b32_e32 v179, v68
	v_mov_b32_e32 v188, v68
	v_mov_b32_e32 v189, v68
	v_mov_b32_e32 v190, v68
	v_mov_b32_e32 v191, v68
	v_mov_b32_e32 v192, v68
	v_mov_b32_e32 v193, v68
	v_mov_b32_e32 v194, v68
	v_mov_b32_e32 v195, v68
	s_branch .LBB0_1709
